# baseline (speedup 1.0000x reference)
.LBB2_12:
	s_or_b64 exec, exec, s[12:13]
	v_lshlrev_b32_e32 v106, 9, v119
	v_ffbl_b32_e32 v107, v107
	v_ffbl_b32_e32 v108, v108
	v_lshlrev_b32_e32 v116, 25, v119
	v_lshl_or_b32 v107, v107, 4, v106
	v_mov_b32_e32 v109, 0x2000
	v_lshl_or_b32 v108, v108, 20, v116
	v_bfrev_b32_e32 v116, 4
	v_ffbl_b32_e32 v0, v0
	v_cndmask_b32_e64 v107, v107, v109, s[8:9]
	v_cndmask_b32_e64 v108, v108, v116, s[4:5]
	v_lshl_or_b32 v0, v0, 4, v106
	v_cndmask_b32_e32 v0, v0, v109, vcc
	v_or_b32_e32 v106, v108, v107
	v_mov_b32_e32 v108, 0x800000
	v_lshlrev_b32_e32 v107, 16, v117
	v_cndmask_b32_e64 v108, 0, v108, s[6:7]
	s_waitcnt lgkmcnt(2)
	v_lshl_or_b32 v0, v118, 24, v0
	v_or3_b32 v0, v0, v108, v107
	ds_write2_b32 v105, v106, v0 offset0:1 offset1:3
	v_cmp_ne_u32_e32 vcc, 0, v140
	v_cmp_ne_u32_e64 s[22:23], 0, v141
	v_lshlrev_b32_e32 v150, 5, v113
	v_lshl_add_u32 v155, v113, 2, v115
	v_lshlrev_b32_e32 v155, 2, v155
	v_add_u32_e32 v155, 0x11840, v155
	v_lshrrev_b64 v[146:147], v150, vcc
	v_lshrrev_b64 v[156:157], v150, s[22:23]
	v_mov_b32_e32 v151, 0x400
	v_cmp_ne_u32_e32 vcc, 0, v146
	v_cmp_ne_u32_e64 s[22:23], 0, v156
	s_nop 1
	v_cndmask_b32_e32 v146, 0, v151, vcc
	v_cndmask_b32_e64 v156, 0, v151, s[22:23]
	v_lshrrev_b64 v[148:149], v150, s[28:29]
	v_lshrrev_b64 v[152:153], v150, s[30:31]
	v_mov_b32_e32 v154, 0x800
	v_cmp_ne_u32_e32 vcc, 0, v148
	v_cmp_ne_u32_e64 s[22:23], 0, v152
	s_nop 1
	v_cndmask_b32_e32 v148, 0, v154, vcc
	v_cndmask_b32_e64 v152, 0, v154, s[22:23]
	v_or_b32_e32 v146, v146, v148
	v_or_b32_e32 v156, v156, v152
	v_lshl_add_u32 v148, v113, 2, v115
	v_lshl_or_b32 v148, v148, 5, v111
	v_lshlrev_b32_e32 v149, 2, v148
	v_add_u32_e32 v149, 0x11040, v149
	v_lshlrev_b32_e32 v148, 4, v148
	ds_read_b32 v152, v149
	ds_read_b32 v153, v149 offset:1024
	s_waitcnt lgkmcnt(0)
	ds_write_b32 v148, v152 offset:57408
	ds_write_b32 v148, v153 offset:61504
	v_cmp_eq_u32_e32 vcc, 0, v111
	s_and_saveexec_b64 s[22:23], vcc
	ds_or_b32 v155, v146
	ds_or_b32 v155, v156 offset:32
	s_or_b64 exec, exec, s[22:23]
	s_movk_i32 s2, 0x2010
	v_mul_u32_u24_e32 v105, 0x2010, v115
	v_cmp_eq_u32_e32 vcc, 0, v114
	s_waitcnt vmcnt(22)
	ds_write_b128 v104, v[38:41] offset:32832
	s_waitcnt vmcnt(21)
	ds_write_b128 v104, v[42:45] offset:36928
	s_waitcnt vmcnt(20)
	ds_write_b128 v104, v[46:49] offset:41024
	s_waitcnt vmcnt(19)
	ds_write_b128 v104, v[50:53] offset:45120
	s_waitcnt vmcnt(18)
	ds_write_b128 v104, v[54:57] offset:49216
	s_waitcnt vmcnt(17)
	ds_write_b128 v104, v[66:69] offset:53312
	s_and_saveexec_b64 s[0:1], vcc
	v_mov_b32_e32 v38, 0
	v_mov_b32_e32 v39, v38
	v_mov_b32_e32 v40, v38
	v_mov_b32_e32 v41, v38
	ds_write_b128 v105, v[38:41] offset:8192
	s_or_b64 exec, exec, s[0:1]
	v_lshlrev_b32_e32 v40, 3, v113
	v_lshlrev_b32_e32 v67, 4, v110
	v_or_b32_e32 v38, 0x1e0, v111
	v_or_b32_e32 v0, 0x8040, v40
	v_mad_u32_u24 v66, v1, s2, v67
	v_mad_u32_u24 v38, v38, 48, v0
	s_waitcnt vmcnt(16)
	ds_write_b128 v66, v[58:61]
	s_waitcnt vmcnt(15)
	ds_write_b128 v66, v[62:65] offset:1024
	s_waitcnt vmcnt(14)
	ds_write_b128 v66, v[70:73] offset:2048
	s_waitcnt vmcnt(13)
	ds_write_b128 v66, v[74:77] offset:3072
	s_waitcnt vmcnt(12)
	ds_write_b128 v66, v[78:81] offset:4096
	s_waitcnt vmcnt(11)
	ds_write_b128 v66, v[82:85] offset:5120
	s_waitcnt vmcnt(10)
	ds_write_b128 v66, v[86:89] offset:6144
	s_waitcnt vmcnt(9)
	ds_write_b128 v66, v[90:93] offset:7168
	v_lshl_add_u32 v116, v113, 3, v105
	v_or_b32_e32 v106, 0x1e0, v111
	v_lshlrev_b32_e32 v138, 4, v106
	v_add_u32_e32 v139, 0x118c0, v138
	v_mul_u32_u24_e32 v156, 48, v106
	v_add_u32_e32 v156, v0, v156
	v_mov_b32_e32 v157, 0x1187c
	v_add_u32_e32 v137, v116, v138
	v_add_u32_e32 v138, 0x200, v138
	v_lshlrev_b32_e32 v160, 4, v111
	v_lshlrev_b32_e32 v161, 3, v111
	v_add_u32_e32 v161, 0x118c0, v161
	v_mul_u32_u24_e32 v162, 48, v111
	v_add_u32_e32 v162, v0, v162
	v_mov_b32_e32 v163, 0x11840
	v_mul_hi_u32_u24_e32 v159, 0x410, v111
	v_mul_u32_u24_e32 v158, 0x410, v111
	v_mov_b32_e32 v107, 0x82000
	v_mad_u64_u32 v[158:159], s[0:1], s20, v107, v[158:159]
	v_lshlrev_b32_e32 v107, 3, v113
	v_or_b32_e32 v158, v158, v107
	v_lshl_add_u64 v[158:159], s[14:15], 0, v[158:159]
	s_mov_b64 s[0:1], 0x79e30
	s_mov_b32 s2, 0xffff7e00
	s_mov_b32 s3, -1
	v_lshl_add_u64 v[158:159], v[158:159], 0, s[0:1]
	v_lshl_add_u32 v107, v114, 2, v163
	v_add_u32_e32 v107, -8, v107
	s_waitcnt lgkmcnt(0)
	s_barrier
	v_add_u32_e32 v194, 0x4c, v67
	ds_read2st64_b32 v[186:187], v194 offset0:224 offset1:228
	ds_read2st64_b32 v[188:189], v194 offset0:232 offset1:236
	ds_read2st64_b32 v[190:191], v194 offset0:240 offset1:244
	ds_read2st64_b32 v[192:193], v194 offset0:248 offset1:252
	ds_read_b128 v[38:41], v138 offset:56896
	ds_read_b128 v[42:45], v139
	ds_read2_b64 v[56:59], v156 offset1:2
	ds_read_b32 v60, v107
	v_add_u32_e32 v156, 0xfffffa00, v156
	ds_read2_b64 v[52:55], v156 offset1:2
	v_add_u32_e32 v106, -2, v114
	v_cmp_gt_u32_e32 vcc, 16, v106
	s_waitcnt lgkmcnt(0)
	v_cndmask_b32_e32 v60, 0, v60, vcc
	s_nop 1
	v_readlane_b32 s4, v60, 17
	v_readlane_b32 s21, v60, 16
	v_add_u32_sdwa v92, v105, v56 dst_sel:DWORD dst_unused:UNUSED_PAD src0_sel:DWORD src1_sel:WORD_0
	v_add_u32_sdwa v93, v105, v56 dst_sel:DWORD dst_unused:UNUSED_PAD src0_sel:DWORD src1_sel:WORD_1
	v_add_u32_sdwa v106, v105, v57 dst_sel:DWORD dst_unused:UNUSED_PAD src0_sel:DWORD src1_sel:WORD_0
	v_add_u32_sdwa v107, v105, v57 dst_sel:DWORD dst_unused:UNUSED_PAD src0_sel:DWORD src1_sel:WORD_1
	v_add_u32_sdwa v108, v105, v58 dst_sel:DWORD dst_unused:UNUSED_PAD src0_sel:DWORD src1_sel:WORD_0
	v_add_u32_sdwa v109, v105, v58 dst_sel:DWORD dst_unused:UNUSED_PAD src0_sel:DWORD src1_sel:WORD_1
	ds_read_b128 v[120:123], v92
	ds_read_b128 v[124:127], v93
	ds_read_b128 v[128:131], v106
	ds_read_b128 v[132:135], v107
	ds_read_b128 v[140:143], v108
	ds_read_b128 v[144:147], v109
	v_add_u32_sdwa v88, v116, v42 dst_sel:DWORD dst_unused:UNUSED_PAD src0_sel:DWORD src1_sel:WORD_0
	v_add_u32_sdwa v89, v116, v42 dst_sel:DWORD dst_unused:UNUSED_PAD src0_sel:DWORD src1_sel:WORD_1
	v_add_u32_sdwa v90, v116, v43 dst_sel:DWORD dst_unused:UNUSED_PAD src0_sel:DWORD src1_sel:WORD_0
	v_add_u32_sdwa v91, v116, v43 dst_sel:DWORD dst_unused:UNUSED_PAD src0_sel:DWORD src1_sel:WORD_1
	v_add_u32_sdwa v173, v116, v44 dst_sel:DWORD dst_unused:UNUSED_PAD src0_sel:DWORD src1_sel:WORD_0
	v_bfe_u32 v117, v41, 16, 7
	v_add_u32_sdwa v118, v116, v39 dst_sel:DWORD dst_unused:UNUSED_PAD src0_sel:DWORD src1_sel:WORD_0
	v_add_u32_sdwa v119, v116, v39 dst_sel:DWORD dst_unused:UNUSED_PAD src0_sel:DWORD src1_sel:WORD_1
	v_add_u32_sdwa v136, v116, v41 dst_sel:DWORD dst_unused:UNUSED_PAD src0_sel:DWORD src1_sel:WORD_0
	s_and_b32 s9, s4, 0xff
	s_waitcnt lgkmcnt(0)
	v_pk_add_f32 v[120:121], v[120:121], v[124:125]
	v_pk_add_f32 v[122:123], v[122:123], v[126:127]
	v_pk_add_f32 v[128:129], v[128:129], v[132:133]
	v_pk_add_f32 v[130:131], v[130:131], v[134:135]
	v_pk_add_f32 v[140:141], v[140:141], v[144:145]
	v_pk_add_f32 v[142:143], v[142:143], v[146:147]
	s_and_b32 s24, s4, 0x900
	s_cbranch_scc1 .Lfarx_pre

.Lchain_done:
.LBB2_44:
	v_mov_b32_e32 v0, 0x10040
	v_lshl_or_b32 v54, v1, 4, v0
	v_lshl_add_u32 v0, v110, 6, v54
	s_waitcnt vmcnt(0)
	ds_write_b128 v0, v[34:37]
	s_add_u32 s0, s16, s18
	s_addc_u32 s1, s17, s19
	v_mul_u32_u24_e32 v195, 0xc00, v110
	v_lshl_add_u32 v195, v98, 4, v195
	v_lshrrev_b32_e32 v186, 24, v186
	v_lshrrev_b32_e32 v187, 24, v187
	v_lshrrev_b32_e32 v188, 24, v188
	v_lshrrev_b32_e32 v189, 24, v189
	v_lshrrev_b32_e32 v190, 24, v190
	v_lshrrev_b32_e32 v191, 24, v191
	v_lshrrev_b32_e32 v192, 24, v192
	v_lshrrev_b32_e32 v193, 24, v193
	v_lshl_add_u32 v186, v186, 6, v54
	v_lshl_add_u32 v187, v187, 6, v54
	v_lshl_add_u32 v188, v188, 6, v54
	v_lshl_add_u32 v189, v189, 6, v54
	v_lshl_add_u32 v190, v190, 6, v54
	v_lshl_add_u32 v191, v191, 6, v54
	v_lshl_add_u32 v192, v192, 6, v54
	v_lshl_add_u32 v193, v193, 6, v54
	s_waitcnt lgkmcnt(0)
	s_barrier
	ds_read_b128 v[120:123], v66
	ds_read_b128 v[152:155], v186
	ds_read_b128 v[124:127], v66 offset:1024
	ds_read_b128 v[156:159], v187
	ds_read_b128 v[128:131], v66 offset:2048
	ds_read_b128 v[160:163], v188
	ds_read_b128 v[132:135], v66 offset:3072
	ds_read_b128 v[164:167], v189
	ds_read_b128 v[136:139], v66 offset:4096
	ds_read_b128 v[168:171], v190
	ds_read_b128 v[140:143], v66 offset:5120
	ds_read_b128 v[172:175], v191
	ds_read_b128 v[144:147], v66 offset:6144
	ds_read_b128 v[176:179], v192
	s_waitcnt lgkmcnt(12)
	ds_read_b128 v[148:151], v66 offset:7168
	ds_read_b128 v[180:183], v193
	s_waitcnt lgkmcnt(14)
	v_pk_add_f32 v[120:121], v[120:121], v[30:31]
	v_pk_add_f32 v[122:123], v[122:123], v[32:33]
	v_pk_add_f32 v[120:121], v[120:121], v[152:153]
	v_pk_add_f32 v[122:123], v[122:123], v[154:155]
	global_store_dwordx4 v195, v[120:123], s[0:1]
	v_add_u32_e32 v195, 0x30000, v195
	s_waitcnt lgkmcnt(12)
	v_pk_add_f32 v[124:125], v[124:125], v[26:27]
	v_pk_add_f32 v[126:127], v[126:127], v[28:29]
	v_pk_add_f32 v[124:125], v[124:125], v[156:157]
	v_pk_add_f32 v[126:127], v[126:127], v[158:159]
	global_store_dwordx4 v195, v[124:127], s[0:1]
	v_add_u32_e32 v195, 0x30000, v195
	s_waitcnt lgkmcnt(10)
	v_pk_add_f32 v[128:129], v[128:129], v[22:23]
	v_pk_add_f32 v[130:131], v[130:131], v[24:25]
	v_pk_add_f32 v[128:129], v[128:129], v[160:161]
	v_pk_add_f32 v[130:131], v[130:131], v[162:163]
	global_store_dwordx4 v195, v[128:131], s[0:1]
	v_add_u32_e32 v195, 0x30000, v195
	s_waitcnt lgkmcnt(8)
	v_pk_add_f32 v[132:133], v[132:133], v[18:19]
	v_pk_add_f32 v[134:135], v[134:135], v[20:21]
	v_pk_add_f32 v[132:133], v[132:133], v[164:165]
	v_pk_add_f32 v[134:135], v[134:135], v[166:167]
	global_store_dwordx4 v195, v[132:135], s[0:1]
	v_add_u32_e32 v195, 0x30000, v195
	s_waitcnt lgkmcnt(6)
	v_pk_add_f32 v[136:137], v[136:137], v[14:15]
	v_pk_add_f32 v[138:139], v[138:139], v[16:17]
	v_pk_add_f32 v[136:137], v[136:137], v[168:169]
	v_pk_add_f32 v[138:139], v[138:139], v[170:171]
	global_store_dwordx4 v195, v[136:139], s[0:1]
	v_add_u32_e32 v195, 0x30000, v195
	s_waitcnt lgkmcnt(4)
	v_pk_add_f32 v[140:141], v[140:141], v[10:11]
	v_pk_add_f32 v[142:143], v[142:143], v[12:13]
	v_pk_add_f32 v[140:141], v[140:141], v[172:173]
	v_pk_add_f32 v[142:143], v[142:143], v[174:175]
	global_store_dwordx4 v195, v[140:143], s[0:1]
	v_add_u32_e32 v195, 0x30000, v195
	s_waitcnt lgkmcnt(2)
	v_pk_add_f32 v[144:145], v[144:145], v[6:7]
	v_pk_add_f32 v[146:147], v[146:147], v[8:9]
	v_pk_add_f32 v[144:145], v[144:145], v[176:177]
	v_pk_add_f32 v[146:147], v[146:147], v[178:179]
	global_store_dwordx4 v195, v[144:147], s[0:1]
	v_add_u32_e32 v195, 0x30000, v195
	s_waitcnt lgkmcnt(0)
	v_pk_add_f32 v[148:149], v[148:149], v[2:3]
	v_pk_add_f32 v[150:151], v[150:151], v[4:5]
	v_pk_add_f32 v[148:149], v[148:149], v[180:181]
	v_pk_add_f32 v[150:151], v[150:151], v[182:183]
	global_store_dwordx4 v195, v[148:151], s[0:1]
	s_endpgm

	.amdhsa_kernel _Z8k3_chainPKfPK15HIP_vector_typeIiLj4EEPKtS6_S0_S0_Pf
		.amdhsa_group_segment_fixed_size 80064
		.amdhsa_private_segment_fixed_size 0
		.amdhsa_kernarg_size 56
		.amdhsa_user_sgpr_count 2
		.amdhsa_user_sgpr_dispatch_ptr 0
		.amdhsa_user_sgpr_queue_ptr 0
		.amdhsa_user_sgpr_kernarg_segment_ptr 1
		.amdhsa_user_sgpr_dispatch_id 0
		.amdhsa_user_sgpr_kernarg_preload_length 0
		.amdhsa_user_sgpr_kernarg_preload_offset 0
		.amdhsa_user_sgpr_private_segment_size 0
		.amdhsa_uses_dynamic_stack 0
		.amdhsa_enable_private_segment 0
		.amdhsa_system_sgpr_workgroup_id_x 1
		.amdhsa_system_sgpr_workgroup_id_y 0
		.amdhsa_system_sgpr_workgroup_id_z 0
		.amdhsa_system_sgpr_workgroup_info 0
		.amdhsa_system_vgpr_workitem_id 0
		.amdhsa_next_free_vgpr 197
		.amdhsa_next_free_sgpr 96
		.amdhsa_accum_offset 196
		.amdhsa_reserve_vcc 1
		.amdhsa_float_round_mode_32 0
		.amdhsa_float_round_mode_16_64 0
		.amdhsa_float_denorm_mode_32 3
		.amdhsa_float_denorm_mode_16_64 3
		.amdhsa_dx10_clamp 1
		.amdhsa_ieee_mode 1
		.amdhsa_fp16_overflow 0
		.amdhsa_tg_split 0
		.amdhsa_exception_fp_ieee_invalid_op 0
		.amdhsa_exception_fp_denorm_src 0
		.amdhsa_exception_fp_ieee_div_zero 0
		.amdhsa_exception_fp_ieee_overflow 0
		.amdhsa_exception_fp_ieee_underflow 0
		.amdhsa_exception_fp_ieee_inexact 0
		.amdhsa_exception_int_div_zero 0
	.end_amdhsa_kernel

amdhsa.kernels:
  - .agpr_count:     0
    .args:
      - .actual_access:  read_only
        .address_space:  global
        .offset:         0
        .size:           8
        .value_kind:     global_buffer
      - .actual_access:  read_only
        .address_space:  global
        .offset:         8
        .size:           8
        .value_kind:     global_buffer
      - .actual_access:  write_only
        .address_space:  global
        .offset:         16
        .size:           8
        .value_kind:     global_buffer
      - .actual_access:  write_only
        .address_space:  global
        .offset:         24
        .size:           8
        .value_kind:     global_buffer
      - .actual_access:  write_only
        .address_space:  global
        .offset:         32
        .size:           8
        .value_kind:     global_buffer
    .group_segment_fixed_size: 1024
    .kernarg_segment_align: 8
    .kernarg_segment_size: 40
    .language:       OpenCL C
    .language_version:
      - 2
      - 0
    .max_flat_workgroup_size: 256
    .name:           _Z7k1_packPKfS0_PmPiP15HIP_vector_typeIfLj4EE
    .private_segment_fixed_size: 0
    .sgpr_count:     16
    .sgpr_spill_count: 0
    .symbol:         _Z7k1_packPKfS0_PmPiP15HIP_vector_typeIfLj4EE.kd
    .uniform_work_group_size: 1
    .uses_dynamic_stack: false
    .vgpr_count:     33
    .vgpr_spill_count: 0
    .wavefront_size: 64
  - .agpr_count:     0
    .args:
      - .actual_access:  read_only
        .address_space:  global
        .offset:         0
        .size:           8
        .value_kind:     global_buffer
      - .actual_access:  read_only
        .address_space:  global
        .offset:         8
        .size:           8
        .value_kind:     global_buffer
      - .actual_access:  write_only
        .address_space:  global
        .offset:         16
        .size:           8
        .value_kind:     global_buffer
      - .actual_access:  read_only
        .address_space:  global
        .offset:         24
        .size:           8
        .value_kind:     global_buffer
      - .actual_access:  write_only
        .address_space:  global
        .offset:         32
        .size:           8
        .value_kind:     global_buffer
      - .actual_access:  write_only
        .address_space:  global
        .offset:         40
        .size:           8
        .value_kind:     global_buffer
      - .actual_access:  read_only
        .address_space:  global
        .offset:         48
        .size:           8
        .value_kind:     global_buffer
      - .address_space:  global
        .offset:         56
        .size:           8
        .value_kind:     global_buffer
      - .actual_access:  write_only
        .address_space:  global
        .offset:         64
        .size:           8
        .value_kind:     global_buffer
      - .actual_access:  write_only
        .address_space:  global
        .offset:         72
        .size:           8
        .value_kind:     global_buffer
    .group_segment_fixed_size: 34880
    .kernarg_segment_align: 8
    .kernarg_segment_size: 80
    .language:       OpenCL C
    .language_version:
      - 2
      - 0
    .max_flat_workgroup_size: 512
    .name:           _Z7k2_elimPKjPKiPiS2_PfP15HIP_vector_typeIiLj4EEPKfS4_PtSA_
    .private_segment_fixed_size: 0
    .sgpr_count:     50
    .sgpr_spill_count: 0
    .symbol:         _Z7k2_elimPKjPKiPiS2_PfP15HIP_vector_typeIiLj4EEPKfS4_PtSA_.kd
    .uniform_work_group_size: 1
    .uses_dynamic_stack: false
    .vgpr_count:     35
    .vgpr_spill_count: 0
    .wavefront_size: 64
  - .agpr_count:     0
    .args:
      - .actual_access:  read_only
        .address_space:  global
        .offset:         0
        .size:           8
        .value_kind:     global_buffer
      - .actual_access:  read_only
        .address_space:  global
        .offset:         8
        .size:           8
        .value_kind:     global_buffer
      - .actual_access:  read_only
        .address_space:  global
        .offset:         16
        .size:           8
        .value_kind:     global_buffer
      - .actual_access:  read_only
        .address_space:  global
        .offset:         24
        .size:           8
        .value_kind:     global_buffer
      - .actual_access:  read_only
        .address_space:  global
        .offset:         32
        .size:           8
        .value_kind:     global_buffer
      - .actual_access:  read_only
        .address_space:  global
        .offset:         40
        .size:           8
        .value_kind:     global_buffer
      - .actual_access:  write_only
        .address_space:  global
        .offset:         48
        .size:           8
        .value_kind:     global_buffer
    .group_segment_fixed_size: 80064
    .kernarg_segment_align: 8
    .kernarg_segment_size: 56
    .language:       OpenCL C
    .language_version:
      - 2
      - 0
    .max_flat_workgroup_size: 256
    .name:           _Z8k3_chainPKfPK15HIP_vector_typeIiLj4EEPKtS6_S0_S0_Pf
    .private_segment_fixed_size: 0
    .sgpr_count:     28
    .sgpr_spill_count: 0
    .symbol:         _Z8k3_chainPKfPK15HIP_vector_typeIiLj4EEPKtS6_S0_S0_Pf.kd
    .uniform_work_group_size: 1
    .uses_dynamic_stack: false
    .vgpr_count:     196
    .vgpr_spill_count: 0
    .wavefront_size: 64
